# conversion in MoE-0 slack, 10 items per wave
# baseline (speedup 1.0000x reference)
.LBB0_1151:
	v_mov_b32_e32 v1, 0x224f0
	ds_read_b32 v1, v1
	s_waitcnt lgkmcnt(0)
	v_readfirstlane_b32 s0, v1
	s_lshl_b32 s0, s0, 2
	s_sub_i32 s0, s0, s33
	s_max_i32 s0, s0, 0
	s_mul_i32 s0, s0, 3
	s_sub_i32 s1, s33, s0
	s_cmp_lt_i32 s1, 1
	s_cbranch_scc1 .Lcv_skip
	s_cmp_lt_i32 s95, s0
	s_cbranch_scc1 .Lcv_skip
	s_lshl_b32 s12, s1, 3
	s_mul_i32 s13, s1, 80
	s_min_i32 s13, s13, 0x1800
	s_sub_i32 s14, s95, s0
	s_lshl_b32 s14, s14, 3
	s_add_i32 s34, s14, s92
	s_addk_i32 s12, 0x200
	s_cmp_ge_i32 s34, s13
	s_cbranch_scc1 .Lcv_skip
	s_mov_b64 s[4:5], -1
	s_cmp_lt_i32 s34, s13
	s_cselect_b64 s[6:7], -1, 0
	s_and_b64 s[8:9], s[6:7], exec
	s_cselect_b32 s16, s34, 0
	s_cmpk_gt_i32 s16, 0xfff
	s_cbranch_scc0 .Lcv1379
	s_bfe_u32 s8, s16, 0x20007
	s_cmp_lt_i32 s8, 1
	s_mov_b32 s17, 4
	s_cbranch_scc1 .Lcv1384
	s_cmp_eq_u32 s8, 1
	s_cbranch_scc1 .Lcv1381
	s_cmp_eq_u32 s8, 2
	s_cselect_b32 s17, 5, 7
	s_mov_b64 s[4:5], 0
	s_branch .Lcv1382

.LBB0_1374:
	s_cmp_lt_i32 s89, 32
	s_cselect_b64 s[6:7], -1, 0
	s_xor_b64 s[8:9], s[16:17], -1
	s_or_b64 s[6:7], s[6:7], s[8:9]
	s_mov_b64 s[4:5], -1
	s_and_b64 vcc, exec, s[6:7]
	s_cbranch_vccnz .LBB0_1443
	s_lshl_b32 s6, s89, 3
	s_add_i32 s6, s6, s92
	s_add_i32 s34, s6, 0xffffff00
	v_mov_b32_e32 v1, 0x224f0
	ds_read_b32 v1, v1
	s_waitcnt lgkmcnt(0)
	v_readfirstlane_b32 s7, v1
	s_lshl_b32 s7, s7, 2
	s_sub_i32 s7, s7, s33
	s_max_i32 s7, s7, 0
	s_mul_i32 s7, s7, 3
	s_sub_i32 s7, s33, s7
	s_max_i32 s7, s7, 0
	s_mul_i32 s7, s7, 80
	s_min_i32 s7, s7, 0x1800
	s_add_i32 s34, s34, s7
	s_cmpk_lt_i32 s34, 0x1800
	s_cselect_b64 s[6:7], -1, 0
	s_and_b64 s[8:9], s[6:7], exec
	s_cselect_b32 s16, s34, 0
	s_cmpk_gt_i32 s16, 0xfff
	s_cbranch_scc0 .LBB0_1379
	s_bfe_u32 s8, s16, 0x20007
	s_cmp_lt_i32 s8, 1
	s_mov_b32 s17, 4
	s_cbranch_scc1 .LBB0_1384
	s_cmp_eq_u32 s8, 1
	s_cbranch_scc1 .LBB0_1381
	s_cmp_eq_u32 s8, 2
	s_cselect_b32 s17, 5, 7
	s_mov_b64 s[4:5], 0
	s_branch .LBB0_1382
